# baseline (speedup 1.0000x reference)
.Lloop_k5:
	s_waitcnt vmcnt(0)
	s_barrier
	ds_read_b128 v[98:101], v94
	ds_read_b128 v[102:105], v94 offset:32768
	ds_read_b128 v[106:109], v94 offset:2048
	ds_read_b128 v[110:113], v94 offset:34816
	ds_read_b128 v[114:117], v94 offset:4096
	ds_read_b128 v[118:121], v94 offset:36864
	ds_read_b128 v[122:125], v94 offset:6144
	ds_read_b128 v[126:129], v94 offset:38912
	ds_read_b128 v[130:133], v95 offset:16384
	ds_read_b128 v[134:137], v95 offset:49152
	s_waitcnt lgkmcnt(1)
	v_mfma_f32_16x16x32_f16 v[62:65], v[98:101], v[130:133], v[62:65]
	ds_read_b128 v[138:141], v95 offset:18432
	ds_read_b128 v[142:145], v95 offset:51200
	s_waitcnt lgkmcnt(2)
	v_mfma_f32_16x16x32_f16 v[62:65], v[98:101], v[134:137], v[62:65]
	ds_read_b128 v[146:149], v95 offset:20480
	ds_read_b128 v[150:153], v95 offset:53248
	v_mfma_f32_16x16x32_f16 v[62:65], v[102:105], v[130:133], v[62:65]
	ds_read_b128 v[154:157], v95 offset:22528
	ds_read_b128 v[158:161], v95 offset:55296
	s_waitcnt lgkmcnt(5)
	v_mfma_f32_16x16x32_f16 v[58:61], v[98:101], v[138:141], v[58:61]
	ds_read_b128 v[162:165], v96
	ds_read_b128 v[166:169], v96 offset:32768
	s_waitcnt lgkmcnt(6)
	v_mfma_f32_16x16x32_f16 v[58:61], v[98:101], v[142:145], v[58:61]
	ds_read_b128 v[170:173], v96 offset:2048
	ds_read_b128 v[174:177], v96 offset:34816
	v_mfma_f32_16x16x32_f16 v[58:61], v[102:105], v[138:141], v[58:61]
	ds_read_b128 v[178:181], v96 offset:4096
	ds_read_b128 v[182:185], v96 offset:36864
	s_waitcnt lgkmcnt(9)
	v_mfma_f32_16x16x32_f16 v[54:57], v[98:101], v[146:149], v[54:57]
	ds_read_b128 v[186:189], v96 offset:6144
	ds_read_b128 v[190:193], v96 offset:38912
	s_waitcnt lgkmcnt(10)
	v_mfma_f32_16x16x32_f16 v[54:57], v[98:101], v[150:153], v[54:57]
	ds_read_b128 v[194:197], v97 offset:16384
	ds_read_b128 v[198:201], v97 offset:49152
	v_mfma_f32_16x16x32_f16 v[54:57], v[102:105], v[146:149], v[54:57]
	ds_read_b128 v[202:205], v97 offset:18432
	ds_read_b128 v[206:209], v97 offset:51200
	s_waitcnt lgkmcnt(13)
	v_mfma_f32_16x16x32_f16 v[50:53], v[98:101], v[154:157], v[50:53]
	ds_read_b128 v[210:213], v97 offset:20480
	ds_read_b128 v[214:217], v97 offset:53248
	s_waitcnt lgkmcnt(14)
	v_mfma_f32_16x16x32_f16 v[50:53], v[98:101], v[158:161], v[50:53]
	ds_read_b128 v[98:101], v97 offset:22528
	ds_read_b128 v[218:221], v97 offset:55296
	v_mfma_f32_16x16x32_f16 v[50:53], v[102:105], v[154:157], v[50:53]
	v_mfma_f32_16x16x32_f16 v[46:49], v[106:109], v[130:133], v[46:49]
	v_mfma_f32_16x16x32_f16 v[46:49], v[106:109], v[134:137], v[46:49]
	v_mfma_f32_16x16x32_f16 v[46:49], v[110:113], v[130:133], v[46:49]
	v_mfma_f32_16x16x32_f16 v[42:45], v[106:109], v[138:141], v[42:45]
	s_add_u32 s28, s28, 0x80
	s_addc_u32 s29, s29, 0
	s_add_u32 s30, s30, 0x80
	s_addc_u32 s31, s31, 0
	s_add_u32 s32, s32, 0x80
	s_addc_u32 s33, s33, 0
	s_add_u32 s34, s34, 0x80
	s_addc_u32 s35, s35, 0
	s_add_i32 s45, s45, -1
	s_cmp_eq_u32 s45, 0
	s_waitcnt lgkmcnt(0)
	s_barrier
	s_cbranch_scc1 .Llast_k5
	s_mov_b64 s[50:51], s[28:29]
	s_mov_b32 m0, s44
	v_mfma_f32_16x16x32_f16 v[42:45], v[106:109], v[142:145], v[42:45]
	global_load_lds_dwordx4 v222, s[50:51]
	v_mfma_f32_16x16x32_f16 v[42:45], v[110:113], v[138:141], v[42:45]
	v_mfma_f32_16x16x32_f16 v[38:41], v[106:109], v[146:149], v[38:41]
	v_mfma_f32_16x16x32_f16 v[38:41], v[106:109], v[150:153], v[38:41]
	v_mfma_f32_16x16x32_f16 v[38:41], v[110:113], v[146:149], v[38:41]
	s_mov_b64 s[52:53], s[32:33]
	s_add_u32 m0, s44, 0x4000
	v_mfma_f32_16x16x32_f16 v[34:37], v[106:109], v[154:157], v[34:37]
	global_load_lds_dwordx4 v223, s[52:53]
	v_mfma_f32_16x16x32_f16 v[34:37], v[106:109], v[158:161], v[34:37]
	v_mfma_f32_16x16x32_f16 v[34:37], v[110:113], v[154:157], v[34:37]
	v_mfma_f32_16x16x32_f16 v[30:33], v[114:117], v[130:133], v[30:33]
	v_mfma_f32_16x16x32_f16 v[30:33], v[114:117], v[134:137], v[30:33]
	s_mov_b64 s[50:51], s[30:31]
	s_add_u32 m0, s44, 0x8000
	v_mfma_f32_16x16x32_f16 v[30:33], v[118:121], v[130:133], v[30:33]
	global_load_lds_dwordx4 v222, s[50:51]
	v_mfma_f32_16x16x32_f16 v[26:29], v[114:117], v[138:141], v[26:29]
	v_mfma_f32_16x16x32_f16 v[26:29], v[114:117], v[142:145], v[26:29]
	v_mfma_f32_16x16x32_f16 v[26:29], v[118:121], v[138:141], v[26:29]
	v_mfma_f32_16x16x32_f16 v[22:25], v[114:117], v[146:149], v[22:25]
	s_mov_b64 s[52:53], s[34:35]
	s_add_u32 m0, s44, 0xc000
	v_mfma_f32_16x16x32_f16 v[22:25], v[114:117], v[150:153], v[22:25]
	global_load_lds_dwordx4 v223, s[52:53]
	v_mfma_f32_16x16x32_f16 v[22:25], v[118:121], v[146:149], v[22:25]
	v_mfma_f32_16x16x32_f16 v[18:21], v[114:117], v[154:157], v[18:21]
	v_mfma_f32_16x16x32_f16 v[18:21], v[114:117], v[158:161], v[18:21]
	v_mfma_f32_16x16x32_f16 v[18:21], v[118:121], v[154:157], v[18:21]
	s_add_u32 s50, s28, s38
	s_addc_u32 s51, s29, 0
	s_add_u32 m0, s44, 0x1000
	v_mfma_f32_16x16x32_f16 v[14:17], v[122:125], v[130:133], v[14:17]
	global_load_lds_dwordx4 v222, s[50:51]
	v_mfma_f32_16x16x32_f16 v[14:17], v[122:125], v[134:137], v[14:17]
	v_mfma_f32_16x16x32_f16 v[14:17], v[126:129], v[130:133], v[14:17]
	v_mfma_f32_16x16x32_f16 v[10:13], v[122:125], v[138:141], v[10:13]
	v_mfma_f32_16x16x32_f16 v[10:13], v[122:125], v[142:145], v[10:13]
	s_add_u32 s52, s32, s41
	s_addc_u32 s53, s33, 0
	s_add_u32 m0, s44, 0x5000
	v_mfma_f32_16x16x32_f16 v[10:13], v[126:129], v[138:141], v[10:13]
	global_load_lds_dwordx4 v223, s[52:53]
	v_mfma_f32_16x16x32_f16 v[6:9], v[122:125], v[146:149], v[6:9]
	v_mfma_f32_16x16x32_f16 v[6:9], v[122:125], v[150:153], v[6:9]
	v_mfma_f32_16x16x32_f16 v[6:9], v[126:129], v[146:149], v[6:9]
	v_mfma_f32_16x16x32_f16 v[2:5], v[122:125], v[154:157], v[2:5]
	s_add_u32 s50, s30, s38
	s_addc_u32 s51, s31, 0
	s_add_u32 m0, s44, 0x9000
	v_mfma_f32_16x16x32_f16 v[2:5], v[122:125], v[158:161], v[2:5]
	global_load_lds_dwordx4 v222, s[50:51]
	v_mfma_f32_16x16x32_f16 v[2:5], v[126:129], v[154:157], v[2:5]
	s_waitcnt lgkmcnt(7)
	v_mfma_f32_16x16x32_f16 v[62:65], v[162:165], v[194:197], v[62:65]
	s_waitcnt lgkmcnt(6)
	v_mfma_f32_16x16x32_f16 v[62:65], v[162:165], v[198:201], v[62:65]
	v_mfma_f32_16x16x32_f16 v[62:65], v[166:169], v[194:197], v[62:65]
	s_add_u32 s52, s34, s41
	s_addc_u32 s53, s35, 0
	s_add_u32 m0, s44, 0xd000
	s_waitcnt lgkmcnt(5)
	v_mfma_f32_16x16x32_f16 v[58:61], v[162:165], v[202:205], v[58:61]
	global_load_lds_dwordx4 v223, s[52:53]
	s_waitcnt lgkmcnt(4)
	v_mfma_f32_16x16x32_f16 v[58:61], v[162:165], v[206:209], v[58:61]
	v_mfma_f32_16x16x32_f16 v[58:61], v[166:169], v[202:205], v[58:61]
	s_waitcnt lgkmcnt(3)
	v_mfma_f32_16x16x32_f16 v[54:57], v[162:165], v[210:213], v[54:57]
	s_waitcnt lgkmcnt(2)
	v_mfma_f32_16x16x32_f16 v[54:57], v[162:165], v[214:217], v[54:57]
	s_add_u32 s50, s28, s39
	s_addc_u32 s51, s29, 0
	s_add_u32 m0, s44, 0x2000
	v_mfma_f32_16x16x32_f16 v[54:57], v[166:169], v[210:213], v[54:57]
	global_load_lds_dwordx4 v222, s[50:51]
	s_waitcnt lgkmcnt(1)
	v_mfma_f32_16x16x32_f16 v[50:53], v[162:165], v[98:101], v[50:53]
	s_waitcnt lgkmcnt(0)
	v_mfma_f32_16x16x32_f16 v[50:53], v[162:165], v[218:221], v[50:53]
	v_mfma_f32_16x16x32_f16 v[50:53], v[166:169], v[98:101], v[50:53]
	v_mfma_f32_16x16x32_f16 v[46:49], v[170:173], v[194:197], v[46:49]
	s_add_u32 s52, s32, s42
	s_addc_u32 s53, s33, 0
	s_add_u32 m0, s44, 0x6000
	v_mfma_f32_16x16x32_f16 v[46:49], v[170:173], v[198:201], v[46:49]
	global_load_lds_dwordx4 v223, s[52:53]
	v_mfma_f32_16x16x32_f16 v[46:49], v[174:177], v[194:197], v[46:49]
	v_mfma_f32_16x16x32_f16 v[42:45], v[170:173], v[202:205], v[42:45]
	v_mfma_f32_16x16x32_f16 v[42:45], v[170:173], v[206:209], v[42:45]
	v_mfma_f32_16x16x32_f16 v[42:45], v[174:177], v[202:205], v[42:45]
	s_add_u32 s50, s30, s39
	s_addc_u32 s51, s31, 0
	s_add_u32 m0, s44, 0xa000
	v_mfma_f32_16x16x32_f16 v[38:41], v[170:173], v[210:213], v[38:41]
	global_load_lds_dwordx4 v222, s[50:51]
	v_mfma_f32_16x16x32_f16 v[38:41], v[170:173], v[214:217], v[38:41]
	v_mfma_f32_16x16x32_f16 v[38:41], v[174:177], v[210:213], v[38:41]
	v_mfma_f32_16x16x32_f16 v[34:37], v[170:173], v[98:101], v[34:37]
	v_mfma_f32_16x16x32_f16 v[34:37], v[170:173], v[218:221], v[34:37]
	s_add_u32 s52, s34, s42
	s_addc_u32 s53, s35, 0
	s_add_u32 m0, s44, 0xe000
	v_mfma_f32_16x16x32_f16 v[34:37], v[174:177], v[98:101], v[34:37]
	global_load_lds_dwordx4 v223, s[52:53]
	v_mfma_f32_16x16x32_f16 v[30:33], v[178:181], v[194:197], v[30:33]
	v_mfma_f32_16x16x32_f16 v[30:33], v[178:181], v[198:201], v[30:33]
	v_mfma_f32_16x16x32_f16 v[30:33], v[182:185], v[194:197], v[30:33]
	v_mfma_f32_16x16x32_f16 v[26:29], v[178:181], v[202:205], v[26:29]
	s_add_u32 s50, s28, s40
	s_addc_u32 s51, s29, 0
	s_add_u32 m0, s44, 0x3000
	v_mfma_f32_16x16x32_f16 v[26:29], v[178:181], v[206:209], v[26:29]
	global_load_lds_dwordx4 v222, s[50:51]
	v_mfma_f32_16x16x32_f16 v[26:29], v[182:185], v[202:205], v[26:29]
	v_mfma_f32_16x16x32_f16 v[22:25], v[178:181], v[210:213], v[22:25]
	v_mfma_f32_16x16x32_f16 v[22:25], v[178:181], v[214:217], v[22:25]
	v_mfma_f32_16x16x32_f16 v[22:25], v[182:185], v[210:213], v[22:25]
	s_add_u32 s52, s32, s43
	s_addc_u32 s53, s33, 0
	s_add_u32 m0, s44, 0x7000
	v_mfma_f32_16x16x32_f16 v[18:21], v[178:181], v[98:101], v[18:21]
	global_load_lds_dwordx4 v223, s[52:53]
	v_mfma_f32_16x16x32_f16 v[18:21], v[178:181], v[218:221], v[18:21]
	v_mfma_f32_16x16x32_f16 v[18:21], v[182:185], v[98:101], v[18:21]
	v_mfma_f32_16x16x32_f16 v[14:17], v[186:189], v[194:197], v[14:17]
	v_mfma_f32_16x16x32_f16 v[14:17], v[186:189], v[198:201], v[14:17]
	s_add_u32 s50, s30, s40
	s_addc_u32 s51, s31, 0
	s_add_u32 m0, s44, 0xb000
	v_mfma_f32_16x16x32_f16 v[14:17], v[190:193], v[194:197], v[14:17]
	global_load_lds_dwordx4 v222, s[50:51]
	v_mfma_f32_16x16x32_f16 v[10:13], v[186:189], v[202:205], v[10:13]
	v_mfma_f32_16x16x32_f16 v[10:13], v[186:189], v[206:209], v[10:13]
	v_mfma_f32_16x16x32_f16 v[10:13], v[190:193], v[202:205], v[10:13]
	v_mfma_f32_16x16x32_f16 v[6:9], v[186:189], v[210:213], v[6:9]
	s_add_u32 s52, s34, s43
	s_addc_u32 s53, s35, 0
	s_add_u32 m0, s44, 0xf000
	v_mfma_f32_16x16x32_f16 v[6:9], v[186:189], v[214:217], v[6:9]
	global_load_lds_dwordx4 v223, s[52:53]
	v_mfma_f32_16x16x32_f16 v[6:9], v[190:193], v[210:213], v[6:9]
	v_mfma_f32_16x16x32_f16 v[2:5], v[186:189], v[98:101], v[2:5]
	v_mfma_f32_16x16x32_f16 v[2:5], v[186:189], v[218:221], v[2:5]
	v_mfma_f32_16x16x32_f16 v[2:5], v[190:193], v[98:101], v[2:5]
	s_branch .Lloop_k5

.Lloop_k6:
	s_add_u32 s28, s28, 0x80
	s_addc_u32 s29, s29, 0
	s_add_u32 s30, s30, 0x80
	s_addc_u32 s31, s31, 0
	s_add_u32 s32, s32, 0x80
	s_addc_u32 s33, s33, 0
	s_add_u32 s34, s34, 0x80
	s_addc_u32 s35, s35, 0
	s_add_i32 s45, s45, -1
	s_cmp_eq_u32 s45, 0
	s_waitcnt vmcnt(0)
	s_barrier
	s_cbranch_scc1 .Llast0_k6
	s_mov_b64 s[50:51], s[28:29]
	s_add_u32 m0, s44, 0x10000
	ds_read_b128 v[98:101], v94
	ds_read_b128 v[102:105], v94 offset:32768
	ds_read_b128 v[106:109], v94 offset:2048
	ds_read_b128 v[110:113], v94 offset:34816
	ds_read_b128 v[114:117], v94 offset:4096
	ds_read_b128 v[118:121], v94 offset:36864
	ds_read_b128 v[122:125], v94 offset:6144
	ds_read_b128 v[126:129], v94 offset:38912
	ds_read_b128 v[130:133], v95 offset:16384
	ds_read_b128 v[134:137], v95 offset:49152
	s_waitcnt lgkmcnt(1)
	v_mfma_f32_16x16x32_f16 v[62:65], v[98:101], v[130:133], v[62:65]
	global_load_lds_dwordx4 v222, s[50:51]
	ds_read_b128 v[138:141], v95 offset:18432
	ds_read_b128 v[142:145], v95 offset:51200
	s_waitcnt lgkmcnt(2)
	v_mfma_f32_16x16x32_f16 v[62:65], v[98:101], v[134:137], v[62:65]
	ds_read_b128 v[146:149], v95 offset:20480
	ds_read_b128 v[150:153], v95 offset:53248
	v_mfma_f32_16x16x32_f16 v[62:65], v[102:105], v[130:133], v[62:65]
	s_mov_b64 s[52:53], s[32:33]
	s_add_u32 m0, s44, 0x14000
	ds_read_b128 v[154:157], v95 offset:22528
	ds_read_b128 v[158:161], v95 offset:55296
	s_waitcnt lgkmcnt(5)
	v_mfma_f32_16x16x32_f16 v[58:61], v[98:101], v[138:141], v[58:61]
	global_load_lds_dwordx4 v223, s[52:53]
	ds_read_b128 v[162:165], v96
	ds_read_b128 v[166:169], v96 offset:32768
	s_waitcnt lgkmcnt(6)
	v_mfma_f32_16x16x32_f16 v[58:61], v[98:101], v[142:145], v[58:61]
	ds_read_b128 v[170:173], v96 offset:2048
	ds_read_b128 v[174:177], v96 offset:34816
	v_mfma_f32_16x16x32_f16 v[58:61], v[102:105], v[138:141], v[58:61]
	s_mov_b64 s[50:51], s[30:31]
	s_add_u32 m0, s44, 0x18000
	ds_read_b128 v[178:181], v96 offset:4096
	ds_read_b128 v[182:185], v96 offset:36864
	s_waitcnt lgkmcnt(9)
	v_mfma_f32_16x16x32_f16 v[54:57], v[98:101], v[146:149], v[54:57]
	global_load_lds_dwordx4 v222, s[50:51]
	ds_read_b128 v[186:189], v96 offset:6144
	ds_read_b128 v[190:193], v96 offset:38912
	s_waitcnt lgkmcnt(10)
	v_mfma_f32_16x16x32_f16 v[54:57], v[98:101], v[150:153], v[54:57]
	ds_read_b128 v[194:197], v97 offset:16384
	ds_read_b128 v[198:201], v97 offset:49152
	v_mfma_f32_16x16x32_f16 v[54:57], v[102:105], v[146:149], v[54:57]
	s_mov_b64 s[52:53], s[34:35]
	s_add_u32 m0, s44, 0x1c000
	ds_read_b128 v[202:205], v97 offset:18432
	ds_read_b128 v[206:209], v97 offset:51200
	s_waitcnt lgkmcnt(13)
	v_mfma_f32_16x16x32_f16 v[50:53], v[98:101], v[154:157], v[50:53]
	global_load_lds_dwordx4 v223, s[52:53]
	ds_read_b128 v[210:213], v97 offset:20480
	ds_read_b128 v[214:217], v97 offset:53248
	s_waitcnt lgkmcnt(14)
	v_mfma_f32_16x16x32_f16 v[50:53], v[98:101], v[158:161], v[50:53]
	ds_read_b128 v[98:101], v97 offset:22528
	ds_read_b128 v[218:221], v97 offset:55296
	v_mfma_f32_16x16x32_f16 v[50:53], v[102:105], v[154:157], v[50:53]
	s_add_u32 s50, s28, s38
	s_addc_u32 s51, s29, 0
	s_add_u32 m0, s44, 0x11000
	v_mfma_f32_16x16x32_f16 v[46:49], v[106:109], v[130:133], v[46:49]
	global_load_lds_dwordx4 v222, s[50:51]
	v_mfma_f32_16x16x32_f16 v[46:49], v[106:109], v[134:137], v[46:49]
	v_mfma_f32_16x16x32_f16 v[46:49], v[110:113], v[130:133], v[46:49]
	s_add_u32 s52, s32, s41
	s_addc_u32 s53, s33, 0
	s_add_u32 m0, s44, 0x15000
	v_mfma_f32_16x16x32_f16 v[42:45], v[106:109], v[138:141], v[42:45]
	global_load_lds_dwordx4 v223, s[52:53]
	v_mfma_f32_16x16x32_f16 v[42:45], v[106:109], v[142:145], v[42:45]
	v_mfma_f32_16x16x32_f16 v[42:45], v[110:113], v[138:141], v[42:45]
	s_add_u32 s50, s30, s38
	s_addc_u32 s51, s31, 0
	s_add_u32 m0, s44, 0x19000
	v_mfma_f32_16x16x32_f16 v[38:41], v[106:109], v[146:149], v[38:41]
	global_load_lds_dwordx4 v222, s[50:51]
	v_mfma_f32_16x16x32_f16 v[38:41], v[106:109], v[150:153], v[38:41]
	v_mfma_f32_16x16x32_f16 v[38:41], v[110:113], v[146:149], v[38:41]
	s_add_u32 s52, s34, s41
	s_addc_u32 s53, s35, 0
	s_add_u32 m0, s44, 0x1d000
	v_mfma_f32_16x16x32_f16 v[34:37], v[106:109], v[154:157], v[34:37]
	global_load_lds_dwordx4 v223, s[52:53]
	v_mfma_f32_16x16x32_f16 v[34:37], v[106:109], v[158:161], v[34:37]
	v_mfma_f32_16x16x32_f16 v[34:37], v[110:113], v[154:157], v[34:37]
	s_add_u32 s50, s28, s39
	s_addc_u32 s51, s29, 0
	s_add_u32 m0, s44, 0x12000
	v_mfma_f32_16x16x32_f16 v[30:33], v[114:117], v[130:133], v[30:33]
	global_load_lds_dwordx4 v222, s[50:51]
	v_mfma_f32_16x16x32_f16 v[30:33], v[114:117], v[134:137], v[30:33]
	v_mfma_f32_16x16x32_f16 v[30:33], v[118:121], v[130:133], v[30:33]
	s_add_u32 s52, s32, s42
	s_addc_u32 s53, s33, 0
	s_add_u32 m0, s44, 0x16000
	v_mfma_f32_16x16x32_f16 v[26:29], v[114:117], v[138:141], v[26:29]
	global_load_lds_dwordx4 v223, s[52:53]
	v_mfma_f32_16x16x32_f16 v[26:29], v[114:117], v[142:145], v[26:29]
	v_mfma_f32_16x16x32_f16 v[26:29], v[118:121], v[138:141], v[26:29]
	s_add_u32 s50, s30, s39
	s_addc_u32 s51, s31, 0
	s_add_u32 m0, s44, 0x1a000
	v_mfma_f32_16x16x32_f16 v[22:25], v[114:117], v[146:149], v[22:25]
	global_load_lds_dwordx4 v222, s[50:51]
	v_mfma_f32_16x16x32_f16 v[22:25], v[114:117], v[150:153], v[22:25]
	v_mfma_f32_16x16x32_f16 v[22:25], v[118:121], v[146:149], v[22:25]
	s_add_u32 s52, s34, s42
	s_addc_u32 s53, s35, 0
	s_add_u32 m0, s44, 0x1e000
	v_mfma_f32_16x16x32_f16 v[18:21], v[114:117], v[154:157], v[18:21]
	global_load_lds_dwordx4 v223, s[52:53]
	v_mfma_f32_16x16x32_f16 v[18:21], v[114:117], v[158:161], v[18:21]
	v_mfma_f32_16x16x32_f16 v[18:21], v[118:121], v[154:157], v[18:21]
	s_add_u32 s50, s28, s40
	s_addc_u32 s51, s29, 0
	s_add_u32 m0, s44, 0x13000
	v_mfma_f32_16x16x32_f16 v[14:17], v[122:125], v[130:133], v[14:17]
	global_load_lds_dwordx4 v222, s[50:51]
	v_mfma_f32_16x16x32_f16 v[14:17], v[122:125], v[134:137], v[14:17]
	v_mfma_f32_16x16x32_f16 v[14:17], v[126:129], v[130:133], v[14:17]
	s_add_u32 s52, s32, s43
	s_addc_u32 s53, s33, 0
	s_add_u32 m0, s44, 0x17000
	v_mfma_f32_16x16x32_f16 v[10:13], v[122:125], v[138:141], v[10:13]
	global_load_lds_dwordx4 v223, s[52:53]
	v_mfma_f32_16x16x32_f16 v[10:13], v[122:125], v[142:145], v[10:13]
	v_mfma_f32_16x16x32_f16 v[10:13], v[126:129], v[138:141], v[10:13]
	s_add_u32 s50, s30, s40
	s_addc_u32 s51, s31, 0
	s_add_u32 m0, s44, 0x1b000
	v_mfma_f32_16x16x32_f16 v[6:9], v[122:125], v[146:149], v[6:9]
	global_load_lds_dwordx4 v222, s[50:51]
	v_mfma_f32_16x16x32_f16 v[6:9], v[122:125], v[150:153], v[6:9]
	v_mfma_f32_16x16x32_f16 v[6:9], v[126:129], v[146:149], v[6:9]
	s_add_u32 s52, s34, s43
	s_addc_u32 s53, s35, 0
	s_add_u32 m0, s44, 0x1f000
	v_mfma_f32_16x16x32_f16 v[2:5], v[122:125], v[154:157], v[2:5]
	global_load_lds_dwordx4 v223, s[52:53]
	v_mfma_f32_16x16x32_f16 v[2:5], v[122:125], v[158:161], v[2:5]
	v_mfma_f32_16x16x32_f16 v[2:5], v[126:129], v[154:157], v[2:5]
	s_waitcnt lgkmcnt(7)
	v_mfma_f32_16x16x32_f16 v[62:65], v[162:165], v[194:197], v[62:65]
	s_waitcnt lgkmcnt(6)
	v_mfma_f32_16x16x32_f16 v[62:65], v[162:165], v[198:201], v[62:65]
	v_mfma_f32_16x16x32_f16 v[62:65], v[166:169], v[194:197], v[62:65]
	s_waitcnt lgkmcnt(5)
	v_mfma_f32_16x16x32_f16 v[58:61], v[162:165], v[202:205], v[58:61]
	s_waitcnt lgkmcnt(4)
	v_mfma_f32_16x16x32_f16 v[58:61], v[162:165], v[206:209], v[58:61]
	v_mfma_f32_16x16x32_f16 v[58:61], v[166:169], v[202:205], v[58:61]
	s_waitcnt lgkmcnt(3)
	v_mfma_f32_16x16x32_f16 v[54:57], v[162:165], v[210:213], v[54:57]
	s_waitcnt lgkmcnt(2)
	v_mfma_f32_16x16x32_f16 v[54:57], v[162:165], v[214:217], v[54:57]
	v_mfma_f32_16x16x32_f16 v[54:57], v[166:169], v[210:213], v[54:57]
	s_waitcnt lgkmcnt(1)
	v_mfma_f32_16x16x32_f16 v[50:53], v[162:165], v[98:101], v[50:53]
	s_waitcnt lgkmcnt(0)
	v_mfma_f32_16x16x32_f16 v[50:53], v[162:165], v[218:221], v[50:53]
	v_mfma_f32_16x16x32_f16 v[50:53], v[166:169], v[98:101], v[50:53]
	v_mfma_f32_16x16x32_f16 v[46:49], v[170:173], v[194:197], v[46:49]
	v_mfma_f32_16x16x32_f16 v[46:49], v[170:173], v[198:201], v[46:49]
	v_mfma_f32_16x16x32_f16 v[46:49], v[174:177], v[194:197], v[46:49]
	v_mfma_f32_16x16x32_f16 v[42:45], v[170:173], v[202:205], v[42:45]
	v_mfma_f32_16x16x32_f16 v[42:45], v[170:173], v[206:209], v[42:45]
	v_mfma_f32_16x16x32_f16 v[42:45], v[174:177], v[202:205], v[42:45]
	v_mfma_f32_16x16x32_f16 v[38:41], v[170:173], v[210:213], v[38:41]
	v_mfma_f32_16x16x32_f16 v[38:41], v[170:173], v[214:217], v[38:41]
	v_mfma_f32_16x16x32_f16 v[38:41], v[174:177], v[210:213], v[38:41]
	v_mfma_f32_16x16x32_f16 v[34:37], v[170:173], v[98:101], v[34:37]
	v_mfma_f32_16x16x32_f16 v[34:37], v[170:173], v[218:221], v[34:37]
	v_mfma_f32_16x16x32_f16 v[34:37], v[174:177], v[98:101], v[34:37]
	v_mfma_f32_16x16x32_f16 v[30:33], v[178:181], v[194:197], v[30:33]
	v_mfma_f32_16x16x32_f16 v[30:33], v[178:181], v[198:201], v[30:33]
	v_mfma_f32_16x16x32_f16 v[30:33], v[182:185], v[194:197], v[30:33]
	v_mfma_f32_16x16x32_f16 v[26:29], v[178:181], v[202:205], v[26:29]
	v_mfma_f32_16x16x32_f16 v[26:29], v[178:181], v[206:209], v[26:29]
	v_mfma_f32_16x16x32_f16 v[26:29], v[182:185], v[202:205], v[26:29]
	v_mfma_f32_16x16x32_f16 v[22:25], v[178:181], v[210:213], v[22:25]
	v_mfma_f32_16x16x32_f16 v[22:25], v[178:181], v[214:217], v[22:25]
	v_mfma_f32_16x16x32_f16 v[22:25], v[182:185], v[210:213], v[22:25]
	v_mfma_f32_16x16x32_f16 v[18:21], v[178:181], v[98:101], v[18:21]
	v_mfma_f32_16x16x32_f16 v[18:21], v[178:181], v[218:221], v[18:21]
	v_mfma_f32_16x16x32_f16 v[18:21], v[182:185], v[98:101], v[18:21]
	v_mfma_f32_16x16x32_f16 v[14:17], v[186:189], v[194:197], v[14:17]
	v_mfma_f32_16x16x32_f16 v[14:17], v[186:189], v[198:201], v[14:17]
	v_mfma_f32_16x16x32_f16 v[14:17], v[190:193], v[194:197], v[14:17]
	v_mfma_f32_16x16x32_f16 v[10:13], v[186:189], v[202:205], v[10:13]
	v_mfma_f32_16x16x32_f16 v[10:13], v[186:189], v[206:209], v[10:13]
	v_mfma_f32_16x16x32_f16 v[10:13], v[190:193], v[202:205], v[10:13]
	v_mfma_f32_16x16x32_f16 v[6:9], v[186:189], v[210:213], v[6:9]
	v_mfma_f32_16x16x32_f16 v[6:9], v[186:189], v[214:217], v[6:9]
	v_mfma_f32_16x16x32_f16 v[6:9], v[190:193], v[210:213], v[6:9]
	v_mfma_f32_16x16x32_f16 v[2:5], v[186:189], v[98:101], v[2:5]
	v_mfma_f32_16x16x32_f16 v[2:5], v[186:189], v[218:221], v[2:5]
	v_mfma_f32_16x16x32_f16 v[2:5], v[190:193], v[98:101], v[2:5]
	s_add_u32 s28, s28, 0x80
	s_addc_u32 s29, s29, 0
	s_add_u32 s30, s30, 0x80
	s_addc_u32 s31, s31, 0
	s_add_u32 s32, s32, 0x80
	s_addc_u32 s33, s33, 0
	s_add_u32 s34, s34, 0x80
	s_addc_u32 s35, s35, 0
	s_add_i32 s45, s45, -1
	s_cmp_eq_u32 s45, 0
	s_waitcnt vmcnt(0)
	s_barrier
	s_cbranch_scc1 .Llast1_k6
	s_mov_b64 s[50:51], s[28:29]
	s_mov_b32 m0, s44
	ds_read_b128 v[98:101], v224
	ds_read_b128 v[102:105], v224 offset:32768
	ds_read_b128 v[106:109], v224 offset:2048
	ds_read_b128 v[110:113], v224 offset:34816
	ds_read_b128 v[114:117], v224 offset:4096
	ds_read_b128 v[118:121], v224 offset:36864
	ds_read_b128 v[122:125], v224 offset:6144
	ds_read_b128 v[126:129], v224 offset:38912
	ds_read_b128 v[130:133], v225 offset:16384
	ds_read_b128 v[134:137], v225 offset:49152
	s_waitcnt lgkmcnt(1)
	v_mfma_f32_16x16x32_f16 v[62:65], v[98:101], v[130:133], v[62:65]
	global_load_lds_dwordx4 v222, s[50:51]
	ds_read_b128 v[138:141], v225 offset:18432
	ds_read_b128 v[142:145], v225 offset:51200
	s_waitcnt lgkmcnt(2)
	v_mfma_f32_16x16x32_f16 v[62:65], v[98:101], v[134:137], v[62:65]
	ds_read_b128 v[146:149], v225 offset:20480
	ds_read_b128 v[150:153], v225 offset:53248
	v_mfma_f32_16x16x32_f16 v[62:65], v[102:105], v[130:133], v[62:65]
	s_mov_b64 s[52:53], s[32:33]
	s_add_u32 m0, s44, 0x4000
	ds_read_b128 v[154:157], v225 offset:22528
	ds_read_b128 v[158:161], v225 offset:55296
	s_waitcnt lgkmcnt(5)
	v_mfma_f32_16x16x32_f16 v[58:61], v[98:101], v[138:141], v[58:61]
	global_load_lds_dwordx4 v223, s[52:53]
	ds_read_b128 v[162:165], v226
	ds_read_b128 v[166:169], v226 offset:32768
	s_waitcnt lgkmcnt(6)
	v_mfma_f32_16x16x32_f16 v[58:61], v[98:101], v[142:145], v[58:61]
	ds_read_b128 v[170:173], v226 offset:2048
	ds_read_b128 v[174:177], v226 offset:34816
	v_mfma_f32_16x16x32_f16 v[58:61], v[102:105], v[138:141], v[58:61]
	s_mov_b64 s[50:51], s[30:31]
	s_add_u32 m0, s44, 0x8000
	ds_read_b128 v[178:181], v226 offset:4096
	ds_read_b128 v[182:185], v226 offset:36864
	s_waitcnt lgkmcnt(9)
	v_mfma_f32_16x16x32_f16 v[54:57], v[98:101], v[146:149], v[54:57]
	global_load_lds_dwordx4 v222, s[50:51]
	ds_read_b128 v[186:189], v226 offset:6144
	ds_read_b128 v[190:193], v226 offset:38912
	s_waitcnt lgkmcnt(10)
	v_mfma_f32_16x16x32_f16 v[54:57], v[98:101], v[150:153], v[54:57]
	ds_read_b128 v[194:197], v227 offset:16384
	ds_read_b128 v[198:201], v227 offset:49152
	v_mfma_f32_16x16x32_f16 v[54:57], v[102:105], v[146:149], v[54:57]
	s_mov_b64 s[52:53], s[34:35]
	s_add_u32 m0, s44, 0xc000
	ds_read_b128 v[202:205], v227 offset:18432
	ds_read_b128 v[206:209], v227 offset:51200
	s_waitcnt lgkmcnt(13)
	v_mfma_f32_16x16x32_f16 v[50:53], v[98:101], v[154:157], v[50:53]
	global_load_lds_dwordx4 v223, s[52:53]
	ds_read_b128 v[210:213], v227 offset:20480
	ds_read_b128 v[214:217], v227 offset:53248
	s_waitcnt lgkmcnt(14)
	v_mfma_f32_16x16x32_f16 v[50:53], v[98:101], v[158:161], v[50:53]
	ds_read_b128 v[98:101], v227 offset:22528
	ds_read_b128 v[218:221], v227 offset:55296
	v_mfma_f32_16x16x32_f16 v[50:53], v[102:105], v[154:157], v[50:53]
	s_add_u32 s50, s28, s38
	s_addc_u32 s51, s29, 0
	s_add_u32 m0, s44, 0x1000
	v_mfma_f32_16x16x32_f16 v[46:49], v[106:109], v[130:133], v[46:49]
	global_load_lds_dwordx4 v222, s[50:51]
	v_mfma_f32_16x16x32_f16 v[46:49], v[106:109], v[134:137], v[46:49]
	v_mfma_f32_16x16x32_f16 v[46:49], v[110:113], v[130:133], v[46:49]
	s_add_u32 s52, s32, s41
	s_addc_u32 s53, s33, 0
	s_add_u32 m0, s44, 0x5000
	v_mfma_f32_16x16x32_f16 v[42:45], v[106:109], v[138:141], v[42:45]
	global_load_lds_dwordx4 v223, s[52:53]
	v_mfma_f32_16x16x32_f16 v[42:45], v[106:109], v[142:145], v[42:45]
	v_mfma_f32_16x16x32_f16 v[42:45], v[110:113], v[138:141], v[42:45]
	s_add_u32 s50, s30, s38
	s_addc_u32 s51, s31, 0
	s_add_u32 m0, s44, 0x9000
	v_mfma_f32_16x16x32_f16 v[38:41], v[106:109], v[146:149], v[38:41]
	global_load_lds_dwordx4 v222, s[50:51]
	v_mfma_f32_16x16x32_f16 v[38:41], v[106:109], v[150:153], v[38:41]
	v_mfma_f32_16x16x32_f16 v[38:41], v[110:113], v[146:149], v[38:41]
	s_add_u32 s52, s34, s41
	s_addc_u32 s53, s35, 0
	s_add_u32 m0, s44, 0xd000
	v_mfma_f32_16x16x32_f16 v[34:37], v[106:109], v[154:157], v[34:37]
	global_load_lds_dwordx4 v223, s[52:53]
	v_mfma_f32_16x16x32_f16 v[34:37], v[106:109], v[158:161], v[34:37]
	v_mfma_f32_16x16x32_f16 v[34:37], v[110:113], v[154:157], v[34:37]
	s_add_u32 s50, s28, s39
	s_addc_u32 s51, s29, 0
	s_add_u32 m0, s44, 0x2000
	v_mfma_f32_16x16x32_f16 v[30:33], v[114:117], v[130:133], v[30:33]
	global_load_lds_dwordx4 v222, s[50:51]
	v_mfma_f32_16x16x32_f16 v[30:33], v[114:117], v[134:137], v[30:33]
	v_mfma_f32_16x16x32_f16 v[30:33], v[118:121], v[130:133], v[30:33]
	s_add_u32 s52, s32, s42
	s_addc_u32 s53, s33, 0
	s_add_u32 m0, s44, 0x6000
	v_mfma_f32_16x16x32_f16 v[26:29], v[114:117], v[138:141], v[26:29]
	global_load_lds_dwordx4 v223, s[52:53]
	v_mfma_f32_16x16x32_f16 v[26:29], v[114:117], v[142:145], v[26:29]
	v_mfma_f32_16x16x32_f16 v[26:29], v[118:121], v[138:141], v[26:29]
	s_add_u32 s50, s30, s39
	s_addc_u32 s51, s31, 0
	s_add_u32 m0, s44, 0xa000
	v_mfma_f32_16x16x32_f16 v[22:25], v[114:117], v[146:149], v[22:25]
	global_load_lds_dwordx4 v222, s[50:51]
	v_mfma_f32_16x16x32_f16 v[22:25], v[114:117], v[150:153], v[22:25]
	v_mfma_f32_16x16x32_f16 v[22:25], v[118:121], v[146:149], v[22:25]
	s_add_u32 s52, s34, s42
	s_addc_u32 s53, s35, 0
	s_add_u32 m0, s44, 0xe000
	v_mfma_f32_16x16x32_f16 v[18:21], v[114:117], v[154:157], v[18:21]
	global_load_lds_dwordx4 v223, s[52:53]
	v_mfma_f32_16x16x32_f16 v[18:21], v[114:117], v[158:161], v[18:21]
	v_mfma_f32_16x16x32_f16 v[18:21], v[118:121], v[154:157], v[18:21]
	s_add_u32 s50, s28, s40
	s_addc_u32 s51, s29, 0
	s_add_u32 m0, s44, 0x3000
	v_mfma_f32_16x16x32_f16 v[14:17], v[122:125], v[130:133], v[14:17]
	global_load_lds_dwordx4 v222, s[50:51]
	v_mfma_f32_16x16x32_f16 v[14:17], v[122:125], v[134:137], v[14:17]
	v_mfma_f32_16x16x32_f16 v[14:17], v[126:129], v[130:133], v[14:17]
	s_add_u32 s52, s32, s43
	s_addc_u32 s53, s33, 0
	s_add_u32 m0, s44, 0x7000
	v_mfma_f32_16x16x32_f16 v[10:13], v[122:125], v[138:141], v[10:13]
	global_load_lds_dwordx4 v223, s[52:53]
	v_mfma_f32_16x16x32_f16 v[10:13], v[122:125], v[142:145], v[10:13]
	v_mfma_f32_16x16x32_f16 v[10:13], v[126:129], v[138:141], v[10:13]
	s_add_u32 s50, s30, s40
	s_addc_u32 s51, s31, 0
	s_add_u32 m0, s44, 0xb000
	v_mfma_f32_16x16x32_f16 v[6:9], v[122:125], v[146:149], v[6:9]
	global_load_lds_dwordx4 v222, s[50:51]
	v_mfma_f32_16x16x32_f16 v[6:9], v[122:125], v[150:153], v[6:9]
	v_mfma_f32_16x16x32_f16 v[6:9], v[126:129], v[146:149], v[6:9]
	s_add_u32 s52, s34, s43
	s_addc_u32 s53, s35, 0
	s_add_u32 m0, s44, 0xf000
	v_mfma_f32_16x16x32_f16 v[2:5], v[122:125], v[154:157], v[2:5]
	global_load_lds_dwordx4 v223, s[52:53]
	v_mfma_f32_16x16x32_f16 v[2:5], v[122:125], v[158:161], v[2:5]
	v_mfma_f32_16x16x32_f16 v[2:5], v[126:129], v[154:157], v[2:5]
	s_waitcnt lgkmcnt(7)
	v_mfma_f32_16x16x32_f16 v[62:65], v[162:165], v[194:197], v[62:65]
	s_waitcnt lgkmcnt(6)
	v_mfma_f32_16x16x32_f16 v[62:65], v[162:165], v[198:201], v[62:65]
	v_mfma_f32_16x16x32_f16 v[62:65], v[166:169], v[194:197], v[62:65]
	s_waitcnt lgkmcnt(5)
	v_mfma_f32_16x16x32_f16 v[58:61], v[162:165], v[202:205], v[58:61]
	s_waitcnt lgkmcnt(4)
	v_mfma_f32_16x16x32_f16 v[58:61], v[162:165], v[206:209], v[58:61]
	v_mfma_f32_16x16x32_f16 v[58:61], v[166:169], v[202:205], v[58:61]
	s_waitcnt lgkmcnt(3)
	v_mfma_f32_16x16x32_f16 v[54:57], v[162:165], v[210:213], v[54:57]
	s_waitcnt lgkmcnt(2)
	v_mfma_f32_16x16x32_f16 v[54:57], v[162:165], v[214:217], v[54:57]
	v_mfma_f32_16x16x32_f16 v[54:57], v[166:169], v[210:213], v[54:57]
	s_waitcnt lgkmcnt(1)
	v_mfma_f32_16x16x32_f16 v[50:53], v[162:165], v[98:101], v[50:53]
	s_waitcnt lgkmcnt(0)
	v_mfma_f32_16x16x32_f16 v[50:53], v[162:165], v[218:221], v[50:53]
	v_mfma_f32_16x16x32_f16 v[50:53], v[166:169], v[98:101], v[50:53]
	v_mfma_f32_16x16x32_f16 v[46:49], v[170:173], v[194:197], v[46:49]
	v_mfma_f32_16x16x32_f16 v[46:49], v[170:173], v[198:201], v[46:49]
	v_mfma_f32_16x16x32_f16 v[46:49], v[174:177], v[194:197], v[46:49]
	v_mfma_f32_16x16x32_f16 v[42:45], v[170:173], v[202:205], v[42:45]
	v_mfma_f32_16x16x32_f16 v[42:45], v[170:173], v[206:209], v[42:45]
	v_mfma_f32_16x16x32_f16 v[42:45], v[174:177], v[202:205], v[42:45]
	v_mfma_f32_16x16x32_f16 v[38:41], v[170:173], v[210:213], v[38:41]
	v_mfma_f32_16x16x32_f16 v[38:41], v[170:173], v[214:217], v[38:41]
	v_mfma_f32_16x16x32_f16 v[38:41], v[174:177], v[210:213], v[38:41]
	v_mfma_f32_16x16x32_f16 v[34:37], v[170:173], v[98:101], v[34:37]
	v_mfma_f32_16x16x32_f16 v[34:37], v[170:173], v[218:221], v[34:37]
	v_mfma_f32_16x16x32_f16 v[34:37], v[174:177], v[98:101], v[34:37]
	v_mfma_f32_16x16x32_f16 v[30:33], v[178:181], v[194:197], v[30:33]
	v_mfma_f32_16x16x32_f16 v[30:33], v[178:181], v[198:201], v[30:33]
	v_mfma_f32_16x16x32_f16 v[30:33], v[182:185], v[194:197], v[30:33]
	v_mfma_f32_16x16x32_f16 v[26:29], v[178:181], v[202:205], v[26:29]
	v_mfma_f32_16x16x32_f16 v[26:29], v[178:181], v[206:209], v[26:29]
	v_mfma_f32_16x16x32_f16 v[26:29], v[182:185], v[202:205], v[26:29]
	v_mfma_f32_16x16x32_f16 v[22:25], v[178:181], v[210:213], v[22:25]
	v_mfma_f32_16x16x32_f16 v[22:25], v[178:181], v[214:217], v[22:25]
	v_mfma_f32_16x16x32_f16 v[22:25], v[182:185], v[210:213], v[22:25]
	v_mfma_f32_16x16x32_f16 v[18:21], v[178:181], v[98:101], v[18:21]
	v_mfma_f32_16x16x32_f16 v[18:21], v[178:181], v[218:221], v[18:21]
	v_mfma_f32_16x16x32_f16 v[18:21], v[182:185], v[98:101], v[18:21]
	v_mfma_f32_16x16x32_f16 v[14:17], v[186:189], v[194:197], v[14:17]
	v_mfma_f32_16x16x32_f16 v[14:17], v[186:189], v[198:201], v[14:17]
	v_mfma_f32_16x16x32_f16 v[14:17], v[190:193], v[194:197], v[14:17]
	v_mfma_f32_16x16x32_f16 v[10:13], v[186:189], v[202:205], v[10:13]
	v_mfma_f32_16x16x32_f16 v[10:13], v[186:189], v[206:209], v[10:13]
	v_mfma_f32_16x16x32_f16 v[10:13], v[190:193], v[202:205], v[10:13]
	v_mfma_f32_16x16x32_f16 v[6:9], v[186:189], v[210:213], v[6:9]
	v_mfma_f32_16x16x32_f16 v[6:9], v[186:189], v[214:217], v[6:9]
	v_mfma_f32_16x16x32_f16 v[6:9], v[190:193], v[210:213], v[6:9]
	v_mfma_f32_16x16x32_f16 v[2:5], v[186:189], v[98:101], v[2:5]
	v_mfma_f32_16x16x32_f16 v[2:5], v[186:189], v[218:221], v[2:5]
	v_mfma_f32_16x16x32_f16 v[2:5], v[190:193], v[98:101], v[2:5]
	s_branch .Lloop_k6

.Lloop_k10:
	s_waitcnt vmcnt(0)
	s_barrier
	ds_read_b128 v[86:89], v82
	ds_read_b128 v[90:93], v82 offset:2048
	ds_read_b128 v[94:97], v82 offset:4096
	ds_read_b128 v[98:101], v82 offset:6144
	ds_read_b128 v[102:105], v83 offset:16384
	ds_read_b128 v[106:109], v83 offset:18432
	s_waitcnt lgkmcnt(1)
	v_mfma_f32_16x16x32_f16 v[62:65], v[86:89], v[102:105], v[62:65]
	ds_read_b128 v[110:113], v83 offset:20480
	ds_read_b128 v[114:117], v83 offset:22528
	s_waitcnt lgkmcnt(2)
	v_mfma_f32_16x16x32_f16 v[58:61], v[86:89], v[106:109], v[58:61]
	ds_read_b128 v[118:121], v84
	ds_read_b128 v[122:125], v84 offset:2048
	s_waitcnt lgkmcnt(3)
	v_mfma_f32_16x16x32_f16 v[54:57], v[86:89], v[110:113], v[54:57]
	ds_read_b128 v[126:129], v84 offset:4096
	ds_read_b128 v[130:133], v84 offset:6144
	s_waitcnt lgkmcnt(4)
	v_mfma_f32_16x16x32_f16 v[50:53], v[86:89], v[114:117], v[50:53]
	ds_read_b128 v[86:89], v85 offset:16384
	ds_read_b128 v[134:137], v85 offset:18432
	v_mfma_f32_16x16x32_f16 v[46:49], v[90:93], v[102:105], v[46:49]
	ds_read_b128 v[138:141], v85 offset:20480
	ds_read_b128 v[142:145], v85 offset:22528
	v_mfma_f32_16x16x32_f16 v[42:45], v[90:93], v[106:109], v[42:45]
	v_mfma_f32_16x16x32_f16 v[38:41], v[90:93], v[110:113], v[38:41]
	v_mfma_f32_16x16x32_f16 v[34:37], v[90:93], v[114:117], v[34:37]
	s_add_u32 s28, s28, 0x80
	s_addc_u32 s29, s29, 0
	s_add_u32 s32, s32, 0x80
	s_addc_u32 s33, s33, 0
	s_add_i32 s45, s45, -1
	s_cmp_eq_u32 s45, 0
	s_waitcnt lgkmcnt(0)
	s_barrier
	s_cbranch_scc1 .Llast_k10
	s_mov_b64 s[50:51], s[28:29]
	s_mov_b32 m0, s44
	v_mfma_f32_16x16x32_f16 v[30:33], v[94:97], v[102:105], v[30:33]
	global_load_lds_dwordx4 v146, s[50:51]
	v_mfma_f32_16x16x32_f16 v[26:29], v[94:97], v[106:109], v[26:29]
	v_mfma_f32_16x16x32_f16 v[22:25], v[94:97], v[110:113], v[22:25]
	s_mov_b64 s[52:53], s[32:33]
	s_add_u32 m0, s44, 0x4000
	v_mfma_f32_16x16x32_f16 v[18:21], v[94:97], v[114:117], v[18:21]
	global_load_lds_dwordx4 v147, s[52:53]
	v_mfma_f32_16x16x32_f16 v[14:17], v[98:101], v[102:105], v[14:17]
	v_mfma_f32_16x16x32_f16 v[10:13], v[98:101], v[106:109], v[10:13]
	s_add_u32 s50, s28, s38
	s_addc_u32 s51, s29, 0
	s_add_u32 m0, s44, 0x1000
	v_mfma_f32_16x16x32_f16 v[6:9], v[98:101], v[110:113], v[6:9]
	global_load_lds_dwordx4 v146, s[50:51]
	v_mfma_f32_16x16x32_f16 v[2:5], v[98:101], v[114:117], v[2:5]
	s_waitcnt lgkmcnt(3)
	v_mfma_f32_16x16x32_f16 v[62:65], v[118:121], v[86:89], v[62:65]
	s_add_u32 s52, s32, s41
	s_addc_u32 s53, s33, 0
	s_add_u32 m0, s44, 0x5000
	s_waitcnt lgkmcnt(2)
	v_mfma_f32_16x16x32_f16 v[58:61], v[118:121], v[134:137], v[58:61]
	global_load_lds_dwordx4 v147, s[52:53]
	s_waitcnt lgkmcnt(1)
	v_mfma_f32_16x16x32_f16 v[54:57], v[118:121], v[138:141], v[54:57]
	s_waitcnt lgkmcnt(0)
	v_mfma_f32_16x16x32_f16 v[50:53], v[118:121], v[142:145], v[50:53]
	s_add_u32 s50, s28, s39
	s_addc_u32 s51, s29, 0
	s_add_u32 m0, s44, 0x2000
	v_mfma_f32_16x16x32_f16 v[46:49], v[122:125], v[86:89], v[46:49]
	global_load_lds_dwordx4 v146, s[50:51]
	v_mfma_f32_16x16x32_f16 v[42:45], v[122:125], v[134:137], v[42:45]
	v_mfma_f32_16x16x32_f16 v[38:41], v[122:125], v[138:141], v[38:41]
	s_add_u32 s52, s32, s42
	s_addc_u32 s53, s33, 0
	s_add_u32 m0, s44, 0x6000
	v_mfma_f32_16x16x32_f16 v[34:37], v[122:125], v[142:145], v[34:37]
	global_load_lds_dwordx4 v147, s[52:53]
	v_mfma_f32_16x16x32_f16 v[30:33], v[126:129], v[86:89], v[30:33]
	v_mfma_f32_16x16x32_f16 v[26:29], v[126:129], v[134:137], v[26:29]
	s_add_u32 s50, s28, s40
	s_addc_u32 s51, s29, 0
	s_add_u32 m0, s44, 0x3000
	v_mfma_f32_16x16x32_f16 v[22:25], v[126:129], v[138:141], v[22:25]
	global_load_lds_dwordx4 v146, s[50:51]
	v_mfma_f32_16x16x32_f16 v[18:21], v[126:129], v[142:145], v[18:21]
	v_mfma_f32_16x16x32_f16 v[14:17], v[130:133], v[86:89], v[14:17]
	s_add_u32 s52, s32, s43
	s_addc_u32 s53, s33, 0
	s_add_u32 m0, s44, 0x7000
	v_mfma_f32_16x16x32_f16 v[10:13], v[130:133], v[134:137], v[10:13]
	global_load_lds_dwordx4 v147, s[52:53]
	v_mfma_f32_16x16x32_f16 v[6:9], v[130:133], v[138:141], v[6:9]
	v_mfma_f32_16x16x32_f16 v[2:5], v[130:133], v[142:145], v[2:5]
	s_branch .Lloop_k10

.Lloop_k12:
	s_waitcnt vmcnt(0)
	s_barrier
	ds_read_b128 v[98:101], v93
	ds_read_b128 v[102:105], v93 offset:32768
	ds_read_b128 v[106:109], v93 offset:2048
	ds_read_b128 v[110:113], v93 offset:34816
	ds_read_b128 v[114:117], v93 offset:4096
	ds_read_b128 v[118:121], v93 offset:36864
	ds_read_b128 v[122:125], v93 offset:6144
	ds_read_b128 v[126:129], v93 offset:38912
	ds_read_b128 v[130:133], v94 offset:16384
	ds_read_b128 v[134:137], v94 offset:49152
	s_waitcnt lgkmcnt(1)
	v_mfma_f32_16x16x32_f16 v[62:65], v[98:101], v[130:133], v[62:65]
	ds_read_b128 v[138:141], v94 offset:18432
	ds_read_b128 v[142:145], v94 offset:51200
	s_waitcnt lgkmcnt(2)
	v_mfma_f32_16x16x32_f16 v[62:65], v[98:101], v[134:137], v[62:65]
	ds_read_b128 v[146:149], v94 offset:20480
	ds_read_b128 v[150:153], v94 offset:53248
	v_mfma_f32_16x16x32_f16 v[62:65], v[102:105], v[130:133], v[62:65]
	ds_read_b128 v[154:157], v94 offset:22528
	ds_read_b128 v[158:161], v94 offset:55296
	s_waitcnt lgkmcnt(5)
	v_mfma_f32_16x16x32_f16 v[58:61], v[98:101], v[138:141], v[58:61]
	ds_read_b128 v[162:165], v95
	ds_read_b128 v[166:169], v95 offset:32768
	s_waitcnt lgkmcnt(6)
	v_mfma_f32_16x16x32_f16 v[58:61], v[98:101], v[142:145], v[58:61]
	ds_read_b128 v[170:173], v95 offset:2048
	ds_read_b128 v[174:177], v95 offset:34816
	v_mfma_f32_16x16x32_f16 v[58:61], v[102:105], v[138:141], v[58:61]
	ds_read_b128 v[178:181], v95 offset:4096
	ds_read_b128 v[182:185], v95 offset:36864
	s_waitcnt lgkmcnt(9)
	v_mfma_f32_16x16x32_f16 v[54:57], v[98:101], v[146:149], v[54:57]
	ds_read_b128 v[186:189], v95 offset:6144
	ds_read_b128 v[190:193], v95 offset:38912
	s_waitcnt lgkmcnt(10)
	v_mfma_f32_16x16x32_f16 v[54:57], v[98:101], v[150:153], v[54:57]
	ds_read_b128 v[194:197], v96 offset:16384
	ds_read_b128 v[198:201], v96 offset:49152
	v_mfma_f32_16x16x32_f16 v[54:57], v[102:105], v[146:149], v[54:57]
	ds_read_b128 v[202:205], v96 offset:18432
	ds_read_b128 v[206:209], v96 offset:51200
	s_waitcnt lgkmcnt(13)
	v_mfma_f32_16x16x32_f16 v[50:53], v[98:101], v[154:157], v[50:53]
	ds_read_b128 v[210:213], v96 offset:20480
	ds_read_b128 v[214:217], v96 offset:53248
	s_waitcnt lgkmcnt(14)
	v_mfma_f32_16x16x32_f16 v[50:53], v[98:101], v[158:161], v[50:53]
	ds_read_b128 v[98:101], v96 offset:22528
	ds_read_b128 v[218:221], v96 offset:55296
	v_mfma_f32_16x16x32_f16 v[50:53], v[102:105], v[154:157], v[50:53]
	v_mfma_f32_16x16x32_f16 v[46:49], v[106:109], v[130:133], v[46:49]
	v_mfma_f32_16x16x32_f16 v[46:49], v[106:109], v[134:137], v[46:49]
	v_mfma_f32_16x16x32_f16 v[46:49], v[110:113], v[130:133], v[46:49]
	v_mfma_f32_16x16x32_f16 v[42:45], v[106:109], v[138:141], v[42:45]
	s_add_u32 s28, s28, 0x80
	s_addc_u32 s29, s29, 0
	s_add_u32 s30, s30, 0x80
	s_addc_u32 s31, s31, 0
	s_add_u32 s32, s32, 0x80
	s_addc_u32 s33, s33, 0
	s_add_u32 s34, s34, 0x80
	s_addc_u32 s35, s35, 0
	s_add_i32 s45, s45, -1
	s_cmp_eq_u32 s45, 0
	s_waitcnt lgkmcnt(0)
	s_barrier
	s_cbranch_scc1 .Llast_k12
	s_mov_b64 s[50:51], s[28:29]
	s_mov_b32 m0, s44
	v_mfma_f32_16x16x32_f16 v[42:45], v[106:109], v[142:145], v[42:45]
	global_load_lds_dwordx4 v222, s[50:51]
	v_mfma_f32_16x16x32_f16 v[42:45], v[110:113], v[138:141], v[42:45]
	v_mfma_f32_16x16x32_f16 v[38:41], v[106:109], v[146:149], v[38:41]
	v_mfma_f32_16x16x32_f16 v[38:41], v[106:109], v[150:153], v[38:41]
	v_mfma_f32_16x16x32_f16 v[38:41], v[110:113], v[146:149], v[38:41]
	s_mov_b64 s[52:53], s[32:33]
	s_add_u32 m0, s44, 0x4000
	v_mfma_f32_16x16x32_f16 v[34:37], v[106:109], v[154:157], v[34:37]
	global_load_lds_dwordx4 v223, s[52:53]
	v_mfma_f32_16x16x32_f16 v[34:37], v[106:109], v[158:161], v[34:37]
	v_mfma_f32_16x16x32_f16 v[34:37], v[110:113], v[154:157], v[34:37]
	v_mfma_f32_16x16x32_f16 v[30:33], v[114:117], v[130:133], v[30:33]
	v_mfma_f32_16x16x32_f16 v[30:33], v[114:117], v[134:137], v[30:33]
	s_mov_b64 s[50:51], s[30:31]
	s_add_u32 m0, s44, 0x8000
	v_mfma_f32_16x16x32_f16 v[30:33], v[118:121], v[130:133], v[30:33]
	global_load_lds_dwordx4 v222, s[50:51]
	v_mfma_f32_16x16x32_f16 v[26:29], v[114:117], v[138:141], v[26:29]
	v_mfma_f32_16x16x32_f16 v[26:29], v[114:117], v[142:145], v[26:29]
	v_mfma_f32_16x16x32_f16 v[26:29], v[118:121], v[138:141], v[26:29]
	v_mfma_f32_16x16x32_f16 v[22:25], v[114:117], v[146:149], v[22:25]
	s_mov_b64 s[52:53], s[34:35]
	s_add_u32 m0, s44, 0xc000
	v_mfma_f32_16x16x32_f16 v[22:25], v[114:117], v[150:153], v[22:25]
	global_load_lds_dwordx4 v223, s[52:53]
	v_mfma_f32_16x16x32_f16 v[22:25], v[118:121], v[146:149], v[22:25]
	v_mfma_f32_16x16x32_f16 v[18:21], v[114:117], v[154:157], v[18:21]
	v_mfma_f32_16x16x32_f16 v[18:21], v[114:117], v[158:161], v[18:21]
	v_mfma_f32_16x16x32_f16 v[18:21], v[118:121], v[154:157], v[18:21]
	s_add_u32 s50, s28, s38
	s_addc_u32 s51, s29, 0
	s_add_u32 m0, s44, 0x1000
	v_mfma_f32_16x16x32_f16 v[14:17], v[122:125], v[130:133], v[14:17]
	global_load_lds_dwordx4 v222, s[50:51]
	v_mfma_f32_16x16x32_f16 v[14:17], v[122:125], v[134:137], v[14:17]
	v_mfma_f32_16x16x32_f16 v[14:17], v[126:129], v[130:133], v[14:17]
	v_mfma_f32_16x16x32_f16 v[10:13], v[122:125], v[138:141], v[10:13]
	v_mfma_f32_16x16x32_f16 v[10:13], v[122:125], v[142:145], v[10:13]
	s_add_u32 s52, s32, s41
	s_addc_u32 s53, s33, 0
	s_add_u32 m0, s44, 0x5000
	v_mfma_f32_16x16x32_f16 v[10:13], v[126:129], v[138:141], v[10:13]
	global_load_lds_dwordx4 v223, s[52:53]
	v_mfma_f32_16x16x32_f16 v[6:9], v[122:125], v[146:149], v[6:9]
	v_mfma_f32_16x16x32_f16 v[6:9], v[122:125], v[150:153], v[6:9]
	v_mfma_f32_16x16x32_f16 v[6:9], v[126:129], v[146:149], v[6:9]
	v_mfma_f32_16x16x32_f16 v[2:5], v[122:125], v[154:157], v[2:5]
	s_add_u32 s50, s30, s38
	s_addc_u32 s51, s31, 0
	s_add_u32 m0, s44, 0x9000
	v_mfma_f32_16x16x32_f16 v[2:5], v[122:125], v[158:161], v[2:5]
	global_load_lds_dwordx4 v222, s[50:51]
	v_mfma_f32_16x16x32_f16 v[2:5], v[126:129], v[154:157], v[2:5]
	s_waitcnt lgkmcnt(7)
	v_mfma_f32_16x16x32_f16 v[62:65], v[162:165], v[194:197], v[62:65]
	s_waitcnt lgkmcnt(6)
	v_mfma_f32_16x16x32_f16 v[62:65], v[162:165], v[198:201], v[62:65]
	v_mfma_f32_16x16x32_f16 v[62:65], v[166:169], v[194:197], v[62:65]
	s_add_u32 s52, s34, s41
	s_addc_u32 s53, s35, 0
	s_add_u32 m0, s44, 0xd000
	s_waitcnt lgkmcnt(5)
	v_mfma_f32_16x16x32_f16 v[58:61], v[162:165], v[202:205], v[58:61]
	global_load_lds_dwordx4 v223, s[52:53]
	s_waitcnt lgkmcnt(4)
	v_mfma_f32_16x16x32_f16 v[58:61], v[162:165], v[206:209], v[58:61]
	v_mfma_f32_16x16x32_f16 v[58:61], v[166:169], v[202:205], v[58:61]
	s_waitcnt lgkmcnt(3)
	v_mfma_f32_16x16x32_f16 v[54:57], v[162:165], v[210:213], v[54:57]
	s_waitcnt lgkmcnt(2)
	v_mfma_f32_16x16x32_f16 v[54:57], v[162:165], v[214:217], v[54:57]
	s_add_u32 s50, s28, s39
	s_addc_u32 s51, s29, 0
	s_add_u32 m0, s44, 0x2000
	v_mfma_f32_16x16x32_f16 v[54:57], v[166:169], v[210:213], v[54:57]
	global_load_lds_dwordx4 v222, s[50:51]
	s_waitcnt lgkmcnt(1)
	v_mfma_f32_16x16x32_f16 v[50:53], v[162:165], v[98:101], v[50:53]
	s_waitcnt lgkmcnt(0)
	v_mfma_f32_16x16x32_f16 v[50:53], v[162:165], v[218:221], v[50:53]
	v_mfma_f32_16x16x32_f16 v[50:53], v[166:169], v[98:101], v[50:53]
	v_mfma_f32_16x16x32_f16 v[46:49], v[170:173], v[194:197], v[46:49]
	s_add_u32 s52, s32, s42
	s_addc_u32 s53, s33, 0
	s_add_u32 m0, s44, 0x6000
	v_mfma_f32_16x16x32_f16 v[46:49], v[170:173], v[198:201], v[46:49]
	global_load_lds_dwordx4 v223, s[52:53]
	v_mfma_f32_16x16x32_f16 v[46:49], v[174:177], v[194:197], v[46:49]
	v_mfma_f32_16x16x32_f16 v[42:45], v[170:173], v[202:205], v[42:45]
	v_mfma_f32_16x16x32_f16 v[42:45], v[170:173], v[206:209], v[42:45]
	v_mfma_f32_16x16x32_f16 v[42:45], v[174:177], v[202:205], v[42:45]
	s_add_u32 s50, s30, s39
	s_addc_u32 s51, s31, 0
	s_add_u32 m0, s44, 0xa000
	v_mfma_f32_16x16x32_f16 v[38:41], v[170:173], v[210:213], v[38:41]
	global_load_lds_dwordx4 v222, s[50:51]
	v_mfma_f32_16x16x32_f16 v[38:41], v[170:173], v[214:217], v[38:41]
	v_mfma_f32_16x16x32_f16 v[38:41], v[174:177], v[210:213], v[38:41]
	v_mfma_f32_16x16x32_f16 v[34:37], v[170:173], v[98:101], v[34:37]
	v_mfma_f32_16x16x32_f16 v[34:37], v[170:173], v[218:221], v[34:37]
	s_add_u32 s52, s34, s42
	s_addc_u32 s53, s35, 0
	s_add_u32 m0, s44, 0xe000
	v_mfma_f32_16x16x32_f16 v[34:37], v[174:177], v[98:101], v[34:37]
	global_load_lds_dwordx4 v223, s[52:53]
	v_mfma_f32_16x16x32_f16 v[30:33], v[178:181], v[194:197], v[30:33]
	v_mfma_f32_16x16x32_f16 v[30:33], v[178:181], v[198:201], v[30:33]
	v_mfma_f32_16x16x32_f16 v[30:33], v[182:185], v[194:197], v[30:33]
	v_mfma_f32_16x16x32_f16 v[26:29], v[178:181], v[202:205], v[26:29]
	s_add_u32 s50, s28, s40
	s_addc_u32 s51, s29, 0
	s_add_u32 m0, s44, 0x3000
	v_mfma_f32_16x16x32_f16 v[26:29], v[178:181], v[206:209], v[26:29]
	global_load_lds_dwordx4 v222, s[50:51]
	v_mfma_f32_16x16x32_f16 v[26:29], v[182:185], v[202:205], v[26:29]
	v_mfma_f32_16x16x32_f16 v[22:25], v[178:181], v[210:213], v[22:25]
	v_mfma_f32_16x16x32_f16 v[22:25], v[178:181], v[214:217], v[22:25]
	v_mfma_f32_16x16x32_f16 v[22:25], v[182:185], v[210:213], v[22:25]
	s_add_u32 s52, s32, s43
	s_addc_u32 s53, s33, 0
	s_add_u32 m0, s44, 0x7000
	v_mfma_f32_16x16x32_f16 v[18:21], v[178:181], v[98:101], v[18:21]
	global_load_lds_dwordx4 v223, s[52:53]
	v_mfma_f32_16x16x32_f16 v[18:21], v[178:181], v[218:221], v[18:21]
	v_mfma_f32_16x16x32_f16 v[18:21], v[182:185], v[98:101], v[18:21]
	v_mfma_f32_16x16x32_f16 v[14:17], v[186:189], v[194:197], v[14:17]
	v_mfma_f32_16x16x32_f16 v[14:17], v[186:189], v[198:201], v[14:17]
	s_add_u32 s50, s30, s40
	s_addc_u32 s51, s31, 0
	s_add_u32 m0, s44, 0xb000
	v_mfma_f32_16x16x32_f16 v[14:17], v[190:193], v[194:197], v[14:17]
	global_load_lds_dwordx4 v222, s[50:51]
	v_mfma_f32_16x16x32_f16 v[10:13], v[186:189], v[202:205], v[10:13]
	v_mfma_f32_16x16x32_f16 v[10:13], v[186:189], v[206:209], v[10:13]
	v_mfma_f32_16x16x32_f16 v[10:13], v[190:193], v[202:205], v[10:13]
	v_mfma_f32_16x16x32_f16 v[6:9], v[186:189], v[210:213], v[6:9]
	s_add_u32 s52, s34, s43
	s_addc_u32 s53, s35, 0
	s_add_u32 m0, s44, 0xf000
	v_mfma_f32_16x16x32_f16 v[6:9], v[186:189], v[214:217], v[6:9]
	global_load_lds_dwordx4 v223, s[52:53]
	v_mfma_f32_16x16x32_f16 v[6:9], v[190:193], v[210:213], v[6:9]
	v_mfma_f32_16x16x32_f16 v[2:5], v[186:189], v[98:101], v[2:5]
	v_mfma_f32_16x16x32_f16 v[2:5], v[186:189], v[218:221], v[2:5]
	v_mfma_f32_16x16x32_f16 v[2:5], v[190:193], v[98:101], v[2:5]
	s_branch .Lloop_k12

.Lloop_k13:
	s_waitcnt vmcnt(0)
	s_barrier
	ds_read_b128 v[86:89], v81
	ds_read_b128 v[90:93], v81 offset:2048
	ds_read_b128 v[94:97], v81 offset:4096
	ds_read_b128 v[98:101], v81 offset:6144
	ds_read_b128 v[102:105], v82 offset:16384
	ds_read_b128 v[106:109], v82 offset:18432
	s_waitcnt lgkmcnt(1)
	v_mfma_f32_16x16x32_f16 v[62:65], v[86:89], v[102:105], v[62:65]
	ds_read_b128 v[110:113], v82 offset:20480
	ds_read_b128 v[114:117], v82 offset:22528
	s_waitcnt lgkmcnt(2)
	v_mfma_f32_16x16x32_f16 v[58:61], v[86:89], v[106:109], v[58:61]
	s_waitcnt lgkmcnt(1)
	v_mfma_f32_16x16x32_f16 v[54:57], v[86:89], v[110:113], v[54:57]
	s_waitcnt lgkmcnt(0)
	v_mfma_f32_16x16x32_f16 v[50:53], v[86:89], v[114:117], v[50:53]
	ds_read_b128 v[86:89], v83
	v_mfma_f32_16x16x32_f16 v[46:49], v[90:93], v[102:105], v[46:49]
	v_mfma_f32_16x16x32_f16 v[42:45], v[90:93], v[106:109], v[42:45]
	v_mfma_f32_16x16x32_f16 v[38:41], v[90:93], v[110:113], v[38:41]
	v_mfma_f32_16x16x32_f16 v[34:37], v[90:93], v[114:117], v[34:37]
	ds_read_b128 v[90:93], v83 offset:2048
	v_mfma_f32_16x16x32_f16 v[30:33], v[94:97], v[102:105], v[30:33]
	v_mfma_f32_16x16x32_f16 v[26:29], v[94:97], v[106:109], v[26:29]
	v_mfma_f32_16x16x32_f16 v[22:25], v[94:97], v[110:113], v[22:25]
	v_mfma_f32_16x16x32_f16 v[18:21], v[94:97], v[114:117], v[18:21]
	ds_read_b128 v[94:97], v83 offset:4096
	v_mfma_f32_16x16x32_f16 v[14:17], v[98:101], v[102:105], v[14:17]
	ds_read_b128 v[102:105], v84 offset:16384
	v_mfma_f32_16x16x32_f16 v[10:13], v[98:101], v[106:109], v[10:13]
	ds_read_b128 v[106:109], v84 offset:18432
	v_mfma_f32_16x16x32_f16 v[6:9], v[98:101], v[110:113], v[6:9]
	ds_read_b128 v[110:113], v84 offset:20480
	v_mfma_f32_16x16x32_f16 v[2:5], v[98:101], v[114:117], v[2:5]
	ds_read_b128 v[98:101], v83 offset:6144
	ds_read_b128 v[114:117], v84 offset:22528
	s_waitcnt lgkmcnt(4)
	v_mfma_f32_16x16x32_f16 v[62:65], v[86:89], v[102:105], v[62:65]
	s_waitcnt lgkmcnt(3)
	v_mfma_f32_16x16x32_f16 v[58:61], v[86:89], v[106:109], v[58:61]
	s_add_u32 s28, s28, 0x80
	s_addc_u32 s29, s29, 0
	s_add_u32 s32, s32, 0x80
	s_addc_u32 s33, s33, 0
	s_add_i32 s45, s45, -1
	s_cmp_eq_u32 s45, 0
	s_waitcnt lgkmcnt(0)
	s_barrier
	s_cbranch_scc1 .Llast_k13
	s_mov_b64 s[50:51], s[28:29]
	s_mov_b32 m0, s44
	s_waitcnt lgkmcnt(2)
	v_mfma_f32_16x16x32_f16 v[54:57], v[86:89], v[110:113], v[54:57]
	global_load_lds_dwordx4 v118, s[50:51]
	s_mov_b64 s[52:53], s[32:33]
	s_add_u32 m0, s44, 0x4000
	s_waitcnt lgkmcnt(0)
	v_mfma_f32_16x16x32_f16 v[50:53], v[86:89], v[114:117], v[50:53]
	global_load_lds_dwordx4 v119, s[52:53]
	s_add_u32 s50, s28, s38
	s_addc_u32 s51, s29, 0
	s_add_u32 m0, s44, 0x1000
	v_mfma_f32_16x16x32_f16 v[46:49], v[90:93], v[102:105], v[46:49]
	global_load_lds_dwordx4 v118, s[50:51]
	s_add_u32 s52, s32, s41
	s_addc_u32 s53, s33, 0
	s_add_u32 m0, s44, 0x5000
	v_mfma_f32_16x16x32_f16 v[42:45], v[90:93], v[106:109], v[42:45]
	global_load_lds_dwordx4 v119, s[52:53]
	s_add_u32 s50, s28, s39
	s_addc_u32 s51, s29, 0
	s_add_u32 m0, s44, 0x2000
	v_mfma_f32_16x16x32_f16 v[38:41], v[90:93], v[110:113], v[38:41]
	global_load_lds_dwordx4 v118, s[50:51]
	s_add_u32 s52, s32, s42
	s_addc_u32 s53, s33, 0
	s_add_u32 m0, s44, 0x6000
	v_mfma_f32_16x16x32_f16 v[34:37], v[90:93], v[114:117], v[34:37]
	global_load_lds_dwordx4 v119, s[52:53]
	s_add_u32 s50, s28, s40
	s_addc_u32 s51, s29, 0
	s_add_u32 m0, s44, 0x3000
	v_mfma_f32_16x16x32_f16 v[30:33], v[94:97], v[102:105], v[30:33]
	global_load_lds_dwordx4 v118, s[50:51]
	s_add_u32 s52, s32, s43
	s_addc_u32 s53, s33, 0
	s_add_u32 m0, s44, 0x7000
	v_mfma_f32_16x16x32_f16 v[26:29], v[94:97], v[106:109], v[26:29]
	global_load_lds_dwordx4 v119, s[52:53]
	v_mfma_f32_16x16x32_f16 v[22:25], v[94:97], v[110:113], v[22:25]
	v_mfma_f32_16x16x32_f16 v[18:21], v[94:97], v[114:117], v[18:21]
	v_mfma_f32_16x16x32_f16 v[14:17], v[98:101], v[102:105], v[14:17]
	v_mfma_f32_16x16x32_f16 v[10:13], v[98:101], v[106:109], v[10:13]
	v_mfma_f32_16x16x32_f16 v[6:9], v[98:101], v[110:113], v[6:9]
	v_mfma_f32_16x16x32_f16 v[2:5], v[98:101], v[114:117], v[2:5]
	s_branch .Lloop_k13
